# gate-up GEMM epilogue (SwiGLU): the three multiplies per element done as packed pairs, elements batched per store group (112 fewer vector instructions per unit-wave)
# baseline (speedup 1.0000x reference)
; __device__ __forceinline__ unsigned pk4_fp8(float a, float b, float c, float d) { int w = 0; w = __builtin_amdgcn_cvt_pk_fp8_f32(a, b, w, false); w = __builtin_amdgcn_cvt_pk_fp8_f32(c, d, w, true); return (unsigned)w; }
; __device__ __forceinline__ float silu_mul(float g, float u) { const float e = __builtin_amdgcn_exp2f(g * -1.4426950408889634f); return g * __builtin_amdgcn_rcpf(1.0f + e) * u; }
;     __device__ __forceinline__ void operator()(const f32x4 (&acc)[2][2][4][2], const Unit& u, int wr, int wc, int fr, int fq) const {
;     ...
;         const int row0 = u.pm * BM + wr * 64 + fr, col0 = u.pn * HALF + wc * 32 + 8 * fq;
; #pragma unroll
;         for (int ai = 0; ai < 2; ++ai)
; #pragma unroll
;             for (int m = 0; m < 4; ++m) { unsigned char* rowp = O + (size_t)(row0 + ai * HALF + m * 16) * ldc + col0;
;                 const f32x4 g0 = acc[ai][0][m][0], g1 = acc[ai][0][m][1], u0 = acc[ai][1][m][0], u1 = acc[ai][1][m][1];
;                 u32x2 w; w.x = pk4_fp8(silu_mul(g0[0], u0[0]), silu_mul(g0[1], u0[1]), silu_mul(g0[2], u0[2]), silu_mul(g0[3], u0[3]));
;                 w.y = pk4_fp8(silu_mul(g1[0], u1[0]), silu_mul(g1[1], u1[1]), silu_mul(g1[2], u1[2]), silu_mul(g1[3], u1[3]));
;                 *(u32x2*)rowp = w; }
.LBB0_1852:
	s_lshl_b32 s15, s42, 8
	v_readlane_b32 s18, v252, 1
	v_mbcnt_lo_u32_b32 v66, -1, 0
	v_mbcnt_hi_u32_b32 v66, -1, v66
	s_add_i32 s15, s15, s18
	v_and_or_b32 v0, v66, 15, s15
	s_lshl_b32 s15, s34, 7
	v_ashrrev_i32_e32 v66, 1, v66
	s_or_b32 s15, s15, s77
	v_and_b32_e32 v66, -8, v66
	v_add_u32_e32 v130, s15, v66
	s_mov_b32 s98, 0xbfb8aa3b
	v_pk_mul_f32 v[66:67], v[126:127], s[98:99] op_sel_hi:[1,0]
	v_pk_mul_f32 v[68:69], v[128:129], s[98:99] op_sel_hi:[1,0]
	v_pk_mul_f32 v[74:75], v[118:119], s[98:99] op_sel_hi:[1,0]
	v_pk_mul_f32 v[76:77], v[120:121], s[98:99] op_sel_hi:[1,0]
	v_exp_f32_e32 v66, v66
	v_exp_f32_e32 v67, v67
	v_exp_f32_e32 v68, v68
	v_exp_f32_e32 v69, v69
	v_exp_f32_e32 v74, v74
	v_exp_f32_e32 v75, v75
	v_exp_f32_e32 v76, v76
	v_exp_f32_e32 v77, v77
	v_add_f32_e32 v66, 1.0, v66
	v_add_f32_e32 v67, 1.0, v67
	v_add_f32_e32 v68, 1.0, v68
	v_add_f32_e32 v69, 1.0, v69
	v_add_f32_e32 v74, 1.0, v74
	v_add_f32_e32 v75, 1.0, v75
	v_add_f32_e32 v76, 1.0, v76
	v_add_f32_e32 v77, 1.0, v77
	v_rcp_f32_e32 v66, v66
	v_rcp_f32_e32 v67, v67
	v_rcp_f32_e32 v68, v68
	v_rcp_f32_e32 v69, v69
	v_rcp_f32_e32 v74, v74
	v_rcp_f32_e32 v75, v75
	v_rcp_f32_e32 v76, v76
	v_rcp_f32_e32 v77, v77
	v_pk_mul_f32 v[66:67], v[126:127], v[66:67]
	v_pk_mul_f32 v[68:69], v[128:129], v[68:69]
	v_pk_mul_f32 v[74:75], v[118:119], v[74:75]
	v_pk_mul_f32 v[76:77], v[120:121], v[76:77]
	v_pk_mul_f32 v[66:67], v[122:123], v[66:67]
	v_pk_mul_f32 v[68:69], v[124:125], v[68:69]
	v_pk_mul_f32 v[74:75], v[114:115], v[74:75]
	v_pk_mul_f32 v[76:77], v[116:117], v[76:77]
	v_cvt_pk_fp8_f32 v66, v66, v67
	v_cvt_pk_fp8_f32 v66, v68, v69 op_sel:[0,0,1]
	v_cvt_pk_fp8_f32 v67, v74, v75
	v_cvt_pk_fp8_f32 v67, v76, v77 op_sel:[0,0,1]
	v_mov_b64_e32 v[132:133], s[0:1]
	v_ashrrev_i32_e32 v131, 31, v130
	v_mad_i64_i32 v[68:69], s[18:19], v0, s78, v[132:133]
	v_lshl_add_u64 v[68:69], v[68:69], 0, v[130:131]
	global_store_dwordx2 v[68:69], v[66:67], off
	v_pk_mul_f32 v[66:67], v[110:111], s[98:99] op_sel_hi:[1,0]
	v_pk_mul_f32 v[68:69], v[112:113], s[98:99] op_sel_hi:[1,0]
	v_pk_mul_f32 v[74:75], v[102:103], s[98:99] op_sel_hi:[1,0]
	v_pk_mul_f32 v[76:77], v[104:105], s[98:99] op_sel_hi:[1,0]
	v_exp_f32_e32 v66, v66
	v_exp_f32_e32 v67, v67
	v_exp_f32_e32 v68, v68
	v_exp_f32_e32 v69, v69
	v_exp_f32_e32 v74, v74
	v_exp_f32_e32 v75, v75
	v_exp_f32_e32 v76, v76
	v_exp_f32_e32 v77, v77
	v_add_f32_e32 v66, 1.0, v66
	v_add_f32_e32 v67, 1.0, v67
	v_add_f32_e32 v68, 1.0, v68
	v_add_f32_e32 v69, 1.0, v69
	v_add_f32_e32 v74, 1.0, v74
	v_add_f32_e32 v75, 1.0, v75
	v_add_f32_e32 v76, 1.0, v76
	v_add_f32_e32 v77, 1.0, v77
	v_rcp_f32_e32 v66, v66
	v_rcp_f32_e32 v67, v67
	v_rcp_f32_e32 v68, v68
	v_rcp_f32_e32 v69, v69
	v_rcp_f32_e32 v74, v74
	v_rcp_f32_e32 v75, v75
	v_rcp_f32_e32 v76, v76
	v_rcp_f32_e32 v77, v77
	v_pk_mul_f32 v[66:67], v[110:111], v[66:67]
	v_pk_mul_f32 v[68:69], v[112:113], v[68:69]
	v_pk_mul_f32 v[74:75], v[102:103], v[74:75]
	v_pk_mul_f32 v[76:77], v[104:105], v[76:77]
	v_pk_mul_f32 v[66:67], v[106:107], v[66:67]
	v_pk_mul_f32 v[68:69], v[108:109], v[68:69]
	v_pk_mul_f32 v[74:75], v[98:99], v[74:75]
	v_pk_mul_f32 v[76:77], v[100:101], v[76:77]
	v_cvt_pk_fp8_f32 v66, v66, v67
	v_cvt_pk_fp8_f32 v66, v68, v69 op_sel:[0,0,1]
	v_cvt_pk_fp8_f32 v67, v74, v75
	v_cvt_pk_fp8_f32 v67, v76, v77 op_sel:[0,0,1]
	v_or_b32_e32 v68, 16, v0
	v_mad_i64_i32 v[68:69], s[18:19], v68, s78, v[132:133]
	v_lshl_add_u64 v[68:69], v[68:69], 0, v[130:131]
	global_store_dwordx2 v[68:69], v[66:67], off
	v_pk_mul_f32 v[66:67], v[94:95], s[98:99] op_sel_hi:[1,0]
	v_pk_mul_f32 v[68:69], v[96:97], s[98:99] op_sel_hi:[1,0]
	v_pk_mul_f32 v[74:75], v[86:87], s[98:99] op_sel_hi:[1,0]
	v_pk_mul_f32 v[76:77], v[88:89], s[98:99] op_sel_hi:[1,0]
	v_exp_f32_e32 v66, v66
	v_exp_f32_e32 v67, v67
	v_exp_f32_e32 v68, v68
	v_exp_f32_e32 v69, v69
	v_exp_f32_e32 v74, v74
	v_exp_f32_e32 v75, v75
	v_exp_f32_e32 v76, v76
	v_exp_f32_e32 v77, v77
	v_add_f32_e32 v66, 1.0, v66
	v_add_f32_e32 v67, 1.0, v67
	v_add_f32_e32 v68, 1.0, v68
	v_add_f32_e32 v69, 1.0, v69
	v_add_f32_e32 v74, 1.0, v74
	v_add_f32_e32 v75, 1.0, v75
	v_add_f32_e32 v76, 1.0, v76
	v_add_f32_e32 v77, 1.0, v77
	v_rcp_f32_e32 v66, v66
	v_rcp_f32_e32 v67, v67
	v_rcp_f32_e32 v68, v68
	v_rcp_f32_e32 v69, v69
	v_rcp_f32_e32 v74, v74
	v_rcp_f32_e32 v75, v75
	v_rcp_f32_e32 v76, v76
	v_rcp_f32_e32 v77, v77
	v_pk_mul_f32 v[66:67], v[94:95], v[66:67]
	v_pk_mul_f32 v[68:69], v[96:97], v[68:69]
	v_pk_mul_f32 v[74:75], v[86:87], v[74:75]
	v_pk_mul_f32 v[76:77], v[88:89], v[76:77]
	v_pk_mul_f32 v[66:67], v[90:91], v[66:67]
	v_pk_mul_f32 v[68:69], v[92:93], v[68:69]
	v_pk_mul_f32 v[74:75], v[82:83], v[74:75]
	v_pk_mul_f32 v[76:77], v[84:85], v[76:77]
	v_cvt_pk_fp8_f32 v66, v66, v67
	v_cvt_pk_fp8_f32 v66, v68, v69 op_sel:[0,0,1]
	v_cvt_pk_fp8_f32 v67, v74, v75
	v_cvt_pk_fp8_f32 v67, v76, v77 op_sel:[0,0,1]
	v_or_b32_e32 v68, 32, v0
	v_mad_i64_i32 v[68:69], s[18:19], v68, s78, v[132:133]
	v_lshl_add_u64 v[68:69], v[68:69], 0, v[130:131]
	global_store_dwordx2 v[68:69], v[66:67], off
	v_pk_mul_f32 v[66:67], v[78:79], s[98:99] op_sel_hi:[1,0]
	v_pk_mul_f32 v[68:69], v[80:81], s[98:99] op_sel_hi:[1,0]
	v_pk_mul_f32 v[74:75], v[70:71], s[98:99] op_sel_hi:[1,0]
	v_pk_mul_f32 v[76:77], v[72:73], s[98:99] op_sel_hi:[1,0]
	v_exp_f32_e32 v66, v66
	v_exp_f32_e32 v67, v67
	v_exp_f32_e32 v68, v68
	v_exp_f32_e32 v69, v69
	v_exp_f32_e32 v74, v74
	v_exp_f32_e32 v75, v75
	v_exp_f32_e32 v76, v76
	v_exp_f32_e32 v77, v77
	v_add_f32_e32 v66, 1.0, v66
	v_add_f32_e32 v67, 1.0, v67
	v_add_f32_e32 v68, 1.0, v68
	v_add_f32_e32 v69, 1.0, v69
	v_add_f32_e32 v74, 1.0, v74
	v_add_f32_e32 v75, 1.0, v75
; __device__ __forceinline__ unsigned pk4_fp8(float a, float b, float c, float d) { int w = 0; w = __builtin_amdgcn_cvt_pk_fp8_f32(a, b, w, false); w = __builtin_amdgcn_cvt_pk_fp8_f32(c, d, w, true); return (unsigned)w; }
; __device__ __forceinline__ float silu_mul(float g, float u) { const float e = __builtin_amdgcn_exp2f(g * -1.4426950408889634f); return g * __builtin_amdgcn_rcpf(1.0f + e) * u; }
;     __device__ __forceinline__ void operator()(const f32x4 (&acc)[2][2][4][2], const Unit& u, int wr, int wc, int fr, int fq) const {
;     ...
;         const int row0 = u.pm * BM + wr * 64 + fr, col0 = u.pn * HALF + wc * 32 + 8 * fq;
; #pragma unroll
;         for (int ai = 0; ai < 2; ++ai)
; #pragma unroll
;             for (int m = 0; m < 4; ++m) { unsigned char* rowp = O + (size_t)(row0 + ai * HALF + m * 16) * ldc + col0;
;                 const f32x4 g0 = acc[ai][0][m][0], g1 = acc[ai][0][m][1], u0 = acc[ai][1][m][0], u1 = acc[ai][1][m][1];
;                 u32x2 w; w.x = pk4_fp8(silu_mul(g0[0], u0[0]), silu_mul(g0[1], u0[1]), silu_mul(g0[2], u0[2]), silu_mul(g0[3], u0[3]));
;                 w.y = pk4_fp8(silu_mul(g1[0], u1[0]), silu_mul(g1[1], u1[1]), silu_mul(g1[2], u1[2]), silu_mul(g1[3], u1[3]));
;                 *(u32x2*)rowp = w; }
	v_add_f32_e32 v76, 1.0, v76
	v_add_f32_e32 v77, 1.0, v77
	v_rcp_f32_e32 v66, v66
	v_rcp_f32_e32 v67, v67
	v_rcp_f32_e32 v68, v68
	v_rcp_f32_e32 v69, v69
	v_rcp_f32_e32 v74, v74
	v_rcp_f32_e32 v75, v75
	v_rcp_f32_e32 v76, v76
	v_rcp_f32_e32 v77, v77
	v_pk_mul_f32 v[66:67], v[78:79], v[66:67]
	v_pk_mul_f32 v[68:69], v[80:81], v[68:69]
	v_pk_mul_f32 v[74:75], v[70:71], v[74:75]
	v_pk_mul_f32 v[76:77], v[72:73], v[76:77]
	v_pk_mul_f32 v[66:67], v[194:195], v[66:67]
	v_pk_mul_f32 v[68:69], v[196:197], v[68:69]
	v_pk_mul_f32 v[74:75], v[204:205], v[74:75]
	v_pk_mul_f32 v[76:77], v[206:207], v[76:77]
	v_cvt_pk_fp8_f32 v66, v66, v67
	v_cvt_pk_fp8_f32 v66, v68, v69 op_sel:[0,0,1]
	v_cvt_pk_fp8_f32 v67, v74, v75
	v_cvt_pk_fp8_f32 v67, v76, v77 op_sel:[0,0,1]
	v_or_b32_e32 v68, 48, v0
	v_mad_i64_i32 v[68:69], s[18:19], v68, s78, v[132:133]
	v_lshl_add_u64 v[68:69], v[68:69], 0, v[130:131]
	global_store_dwordx2 v[68:69], v[66:67], off
	v_pk_mul_f32 v[66:67], v[62:63], s[98:99] op_sel_hi:[1,0]
	v_pk_mul_f32 v[68:69], v[64:65], s[98:99] op_sel_hi:[1,0]
	v_pk_mul_f32 v[74:75], v[54:55], s[98:99] op_sel_hi:[1,0]
	v_pk_mul_f32 v[76:77], v[56:57], s[98:99] op_sel_hi:[1,0]
	v_exp_f32_e32 v66, v66
	v_exp_f32_e32 v67, v67
	v_exp_f32_e32 v68, v68
	v_exp_f32_e32 v69, v69
	v_exp_f32_e32 v74, v74
	v_exp_f32_e32 v75, v75
	v_exp_f32_e32 v76, v76
	v_exp_f32_e32 v77, v77
	v_add_f32_e32 v66, 1.0, v66
	v_add_f32_e32 v67, 1.0, v67
	v_add_f32_e32 v68, 1.0, v68
	v_add_f32_e32 v69, 1.0, v69
	v_add_f32_e32 v74, 1.0, v74
	v_add_f32_e32 v75, 1.0, v75
	v_add_f32_e32 v76, 1.0, v76
	v_add_f32_e32 v77, 1.0, v77
	v_rcp_f32_e32 v66, v66
	v_rcp_f32_e32 v67, v67
	v_rcp_f32_e32 v68, v68
	v_rcp_f32_e32 v69, v69
	v_rcp_f32_e32 v74, v74
	v_rcp_f32_e32 v75, v75
	v_rcp_f32_e32 v76, v76
	v_rcp_f32_e32 v77, v77
	v_pk_mul_f32 v[66:67], v[62:63], v[66:67]
	v_pk_mul_f32 v[68:69], v[64:65], v[68:69]
	v_pk_mul_f32 v[74:75], v[54:55], v[74:75]
	v_pk_mul_f32 v[76:77], v[56:57], v[76:77]
	v_pk_mul_f32 v[66:67], v[58:59], v[66:67]
	v_pk_mul_f32 v[68:69], v[60:61], v[68:69]
	v_pk_mul_f32 v[74:75], v[50:51], v[74:75]
	v_pk_mul_f32 v[76:77], v[52:53], v[76:77]
	v_cvt_pk_fp8_f32 v58, v66, v67
	v_cvt_pk_fp8_f32 v58, v68, v69 op_sel:[0,0,1]
	v_cvt_pk_fp8_f32 v59, v74, v75
	v_cvt_pk_fp8_f32 v59, v76, v77 op_sel:[0,0,1]
	v_add_u32_e32 v68, 0x80, v0
	s_andn2_b64 vcc, exec, s[40:41]
	v_mad_i64_i32 v[50:51], s[18:19], v68, s78, v[132:133]
	v_lshl_add_u64 v[50:51], v[50:51], 0, v[130:131]
	global_store_dwordx2 v[50:51], v[58:59], off
	v_pk_mul_f32 v[66:67], v[46:47], s[98:99] op_sel_hi:[1,0]
	v_pk_mul_f32 v[68:69], v[48:49], s[98:99] op_sel_hi:[1,0]
	v_pk_mul_f32 v[74:75], v[38:39], s[98:99] op_sel_hi:[1,0]
	v_pk_mul_f32 v[76:77], v[40:41], s[98:99] op_sel_hi:[1,0]
	v_exp_f32_e32 v66, v66
	v_exp_f32_e32 v67, v67
	v_exp_f32_e32 v68, v68
	v_exp_f32_e32 v69, v69
	v_exp_f32_e32 v74, v74
	v_exp_f32_e32 v75, v75
	v_exp_f32_e32 v76, v76
	v_exp_f32_e32 v77, v77
	v_add_f32_e32 v66, 1.0, v66
	v_add_f32_e32 v67, 1.0, v67
	v_add_f32_e32 v68, 1.0, v68
	v_add_f32_e32 v69, 1.0, v69
	v_add_f32_e32 v74, 1.0, v74
	v_add_f32_e32 v75, 1.0, v75
	v_add_f32_e32 v76, 1.0, v76
	v_add_f32_e32 v77, 1.0, v77
	v_rcp_f32_e32 v66, v66
	v_rcp_f32_e32 v67, v67
	v_rcp_f32_e32 v68, v68
	v_rcp_f32_e32 v69, v69
	v_rcp_f32_e32 v74, v74
	v_rcp_f32_e32 v75, v75
	v_rcp_f32_e32 v76, v76
	v_rcp_f32_e32 v77, v77
	v_pk_mul_f32 v[66:67], v[46:47], v[66:67]
	v_pk_mul_f32 v[68:69], v[48:49], v[68:69]
	v_pk_mul_f32 v[74:75], v[38:39], v[74:75]
	v_pk_mul_f32 v[76:77], v[40:41], v[76:77]
	v_pk_mul_f32 v[66:67], v[42:43], v[66:67]
	v_pk_mul_f32 v[68:69], v[44:45], v[68:69]
; __device__ __forceinline__ int lane_id() { int l; asm volatile("v_mbcnt_lo_u32_b32 %0, -1, 0\n\tv_mbcnt_hi_u32_b32 %0, -1, %0" : "=v"(l)); return l; }
; __device__ __forceinline__ unsigned pk4_fp8(float a, float b, float c, float d) { int w = 0; w = __builtin_amdgcn_cvt_pk_fp8_f32(a, b, w, false); w = __builtin_amdgcn_cvt_pk_fp8_f32(c, d, w, true); return (unsigned)w; }
; __device__ __forceinline__ float silu_mul(float g, float u) { const float e = __builtin_amdgcn_exp2f(g * -1.4426950408889634f); return g * __builtin_amdgcn_rcpf(1.0f + e) * u; }
; #define PG8_BAR __builtin_amdgcn_s_barrier()
;     __device__ __forceinline__ void operator()(const f32x4 (&acc)[2][2][4][2], const Unit& u, int wr, int wc, int fr, int fq) const {
;     ...
;         const int row0 = u.pm * BM + wr * 64 + fr, col0 = u.pn * HALF + wc * 32 + 8 * fq;
; #pragma unroll
;         for (int ai = 0; ai < 2; ++ai)
; #pragma unroll
;             for (int m = 0; m < 4; ++m) { unsigned char* rowp = O + (size_t)(row0 + ai * HALF + m * 16) * ldc + col0;
;                 const f32x4 g0 = acc[ai][0][m][0], g1 = acc[ai][0][m][1], u0 = acc[ai][1][m][0], u1 = acc[ai][1][m][1];
;                 u32x2 w; w.x = pk4_fp8(silu_mul(g0[0], u0[0]), silu_mul(g0[1], u0[1]), silu_mul(g0[2], u0[2]), silu_mul(g0[3], u0[3]));
;                 w.y = pk4_fp8(silu_mul(g1[0], u1[0]), silu_mul(g1[1], u1[1]), silu_mul(g1[2], u1[2]), silu_mul(g1[3], u1[3]));
;                 *(u32x2*)rowp = w; }
; template <class Epi, class Sched, bool ALIGN_EPI = false, bool SP2 = false, bool FP8 = false>
; __device__ __forceinline__ void gemm_phase(PG8_LAS unsigned char* lds, const Gemm g, const Sched& S, const Epi& E, const int wave_) {
;     ...
;         if constexpr (ALIGN_EPI) { if (wr == 0) PG8_BAR; }
;         if constexpr (!Epi::AFTER_DRAIN) { const int l2_ = lane_id(); E(acc, cur, wr, wc, l2_ & 15, l2_ >> 4); S.done(cur); }
;         if (!has_next) break;
	v_pk_mul_f32 v[74:75], v[34:35], v[74:75]
	v_pk_mul_f32 v[76:77], v[36:37], v[76:77]
	v_cvt_pk_fp8_f32 v42, v66, v67
	v_cvt_pk_fp8_f32 v42, v68, v69 op_sel:[0,0,1]
	v_cvt_pk_fp8_f32 v43, v74, v75
	v_cvt_pk_fp8_f32 v43, v76, v77 op_sel:[0,0,1]
	v_add_u32_e32 v52, 0x90, v0
	v_mad_i64_i32 v[34:35], s[18:19], v52, s78, v[132:133]
	v_lshl_add_u64 v[34:35], v[34:35], 0, v[130:131]
	global_store_dwordx2 v[34:35], v[42:43], off
	v_pk_mul_f32 v[66:67], v[30:31], s[98:99] op_sel_hi:[1,0]
	v_pk_mul_f32 v[68:69], v[32:33], s[98:99] op_sel_hi:[1,0]
	v_pk_mul_f32 v[74:75], v[22:23], s[98:99] op_sel_hi:[1,0]
	v_pk_mul_f32 v[76:77], v[24:25], s[98:99] op_sel_hi:[1,0]
	v_exp_f32_e32 v66, v66
	v_exp_f32_e32 v67, v67
	v_exp_f32_e32 v68, v68
	v_exp_f32_e32 v69, v69
	v_exp_f32_e32 v74, v74
	v_exp_f32_e32 v75, v75
	v_exp_f32_e32 v76, v76
	v_exp_f32_e32 v77, v77
	v_add_f32_e32 v66, 1.0, v66
	v_add_f32_e32 v67, 1.0, v67
	v_add_f32_e32 v68, 1.0, v68
	v_add_f32_e32 v69, 1.0, v69
	v_add_f32_e32 v74, 1.0, v74
	v_add_f32_e32 v75, 1.0, v75
	v_add_f32_e32 v76, 1.0, v76
	v_add_f32_e32 v77, 1.0, v77
	v_rcp_f32_e32 v66, v66
	v_rcp_f32_e32 v67, v67
	v_rcp_f32_e32 v68, v68
	v_rcp_f32_e32 v69, v69
	v_rcp_f32_e32 v74, v74
	v_rcp_f32_e32 v75, v75
	v_rcp_f32_e32 v76, v76
	v_rcp_f32_e32 v77, v77
	v_pk_mul_f32 v[66:67], v[30:31], v[66:67]
	v_pk_mul_f32 v[68:69], v[32:33], v[68:69]
	v_pk_mul_f32 v[74:75], v[22:23], v[74:75]
	v_pk_mul_f32 v[76:77], v[24:25], v[76:77]
	v_pk_mul_f32 v[66:67], v[26:27], v[66:67]
	v_pk_mul_f32 v[68:69], v[28:29], v[68:69]
	v_pk_mul_f32 v[74:75], v[18:19], v[74:75]
	v_pk_mul_f32 v[76:77], v[20:21], v[76:77]
	v_cvt_pk_fp8_f32 v26, v66, v67
	v_cvt_pk_fp8_f32 v26, v68, v69 op_sel:[0,0,1]
	v_cvt_pk_fp8_f32 v27, v74, v75
	v_cvt_pk_fp8_f32 v27, v76, v77 op_sel:[0,0,1]
	v_add_u32_e32 v36, 0xa0, v0
	v_add_u32_e32 v0, 0xb0, v0
	v_mad_i64_i32 v[18:19], s[18:19], v36, s78, v[132:133]
	v_lshl_add_u64 v[18:19], v[18:19], 0, v[130:131]
	global_store_dwordx2 v[18:19], v[26:27], off
	v_pk_mul_f32 v[66:67], v[14:15], s[98:99] op_sel_hi:[1,0]
	v_pk_mul_f32 v[68:69], v[16:17], s[98:99] op_sel_hi:[1,0]
	v_pk_mul_f32 v[74:75], v[6:7], s[98:99] op_sel_hi:[1,0]
	v_pk_mul_f32 v[76:77], v[8:9], s[98:99] op_sel_hi:[1,0]
	v_exp_f32_e32 v66, v66
	v_exp_f32_e32 v67, v67
	v_exp_f32_e32 v68, v68
	v_exp_f32_e32 v69, v69
	v_exp_f32_e32 v74, v74
	v_exp_f32_e32 v75, v75
	v_exp_f32_e32 v76, v76
	v_exp_f32_e32 v77, v77
	v_add_f32_e32 v66, 1.0, v66
	v_add_f32_e32 v67, 1.0, v67
	v_add_f32_e32 v68, 1.0, v68
	v_add_f32_e32 v69, 1.0, v69
	v_add_f32_e32 v74, 1.0, v74
	v_add_f32_e32 v75, 1.0, v75
	v_add_f32_e32 v76, 1.0, v76
	v_add_f32_e32 v77, 1.0, v77
	v_rcp_f32_e32 v66, v66
	v_rcp_f32_e32 v67, v67
	v_rcp_f32_e32 v68, v68
	v_rcp_f32_e32 v69, v69
	v_rcp_f32_e32 v74, v74
	v_rcp_f32_e32 v75, v75
	v_rcp_f32_e32 v76, v76
	v_rcp_f32_e32 v77, v77
	v_pk_mul_f32 v[66:67], v[14:15], v[66:67]
	v_pk_mul_f32 v[68:69], v[16:17], v[68:69]
	v_pk_mul_f32 v[74:75], v[6:7], v[74:75]
	v_pk_mul_f32 v[76:77], v[8:9], v[76:77]
	v_pk_mul_f32 v[66:67], v[10:11], v[66:67]
	v_pk_mul_f32 v[68:69], v[12:13], v[68:69]
	v_pk_mul_f32 v[74:75], v[2:3], v[74:75]
	v_pk_mul_f32 v[76:77], v[4:5], v[76:77]
	v_cvt_pk_fp8_f32 v10, v66, v67
	v_cvt_pk_fp8_f32 v10, v68, v69 op_sel:[0,0,1]
	v_cvt_pk_fp8_f32 v11, v74, v75
	v_cvt_pk_fp8_f32 v11, v76, v77 op_sel:[0,0,1]
	v_mad_i64_i32 v[2:3], s[18:19], v0, s78, v[132:133]
	v_lshl_add_u64 v[2:3], v[2:3], 0, v[130:131]
	s_mov_b64 s[18:19], -1
	global_store_dwordx2 v[2:3], v[10:11], off
	s_cbranch_vccnz .LBB0_1837
	s_and_b64 vcc, exec, s[38:39]
	s_cbranch_vccnz .LBB0_1836
	s_barrier
	s_branch .LBB0_1836
